# MoE GEMM K loops: per-segment s_setprio flips replaced by one static priority raise for waves 4-7 (section 6.3 lever on the 8-phase template)
# baseline (speedup 1.0000x reference)
.LBB0_1782:
	s_cmp_lg_u32 s14, 1
	s_cbranch_scc1 .Lmoe1_prio_skip
	s_setprio 1

.LBB0_1787:
	s_lshl_b32 s20, s63, 10
	s_add_i32 s20, s20, 0
	s_add_i32 s20, s20, 0x20800
	s_add_u32 s68, s18, 0x100
	v_lshl_add_u32 v209, v170, 2, s20
	v_lshl_add_u32 v210, v171, 2, s20
	s_addc_u32 s69, s19, 0
	s_mov_b32 s70, -2
	s_mov_b64 s[18:19], s[10:11]
	ds_read_b32 v0, v209 offset:512
	ds_read_b32 v166, v210 offset:512
	ds_read_b128 v[22:25], v186
	ds_read_b128 v[18:21], v175
	ds_read_b128 v[26:29], v176
	ds_read_b128 v[30:33], v187
	ds_read_b128 v[6:9], v188
	ds_read_b128 v[2:5], v177
	ds_read_b128 v[10:13], v178
	ds_read_b128 v[14:17], v189
	s_add_u32 s22, s18, 0x80
	s_addc_u32 s23, s19, 0
	s_cmp_eq_u32 s70, 4
	s_cselect_b64 s[24:25], -1, 0
	s_and_b64 s[20:21], s[24:25], exec
	s_cselect_b32 s21, s5, s23
	s_cselect_b32 s20, s4, s22
	s_cselect_b32 s22, s14, s68
	s_cselect_b32 s23, s15, s69
	s_and_b64 s[24:25], s[16:17], s[24:25]
	v_add_u32_e32 v211, 0, v174
	s_waitcnt lgkmcnt(0)
	v_lshl_or_b32 v0, v0, 10, v173
	s_add_i32 m0, s31, 0xc000
	ds_read_b128 v[230:233], v211
	ds_read_b128 v[238:241], v211 offset:2048
	ds_read_b128 v[234:237], v190
	ds_read_b128 v[242:245], v190 offset:2048
	ds_read_b128 v[246:249], v211 offset:4096
	ds_read_b128 v[222:225], v211 offset:6144
	ds_read_b128 v[250:253], v190 offset:4096
	ds_read_b128 v[226:229], v190 offset:6144
	global_load_lds_dwordx4 v0, s[18:19]
	v_lshl_or_b32 v0, v166, 10, v173
	s_add_i32 m0, s31, 0xe000
	s_nop 0
	global_load_lds_dwordx4 v0, s[18:19]
	s_waitcnt vmcnt(8)
	s_waitcnt lgkmcnt(0)
	s_barrier
	s_waitcnt lgkmcnt(0)
	v_mfma_scale_f32_16x16x128_f8f6f4 v[158:161], v[18:25], v[230:237], 0, v172, v172 op_sel_hi:[0,0,0]
	v_mfma_scale_f32_16x16x128_f8f6f4 v[150:153], v[26:33], v[230:237], 0, v172, v172 op_sel_hi:[0,0,0]
	v_mfma_scale_f32_16x16x128_f8f6f4 v[142:145], v[18:25], v[238:245], 0, v172, v172 op_sel_hi:[0,0,0]
	v_mfma_scale_f32_16x16x128_f8f6f4 v[134:137], v[26:33], v[238:245], 0, v172, v172 op_sel_hi:[0,0,0]
	v_mfma_scale_f32_16x16x128_f8f6f4 v[126:129], v[18:25], v[246:253], 0, v172, v172 op_sel_hi:[0,0,0]
	v_mfma_scale_f32_16x16x128_f8f6f4 v[118:121], v[26:33], v[246:253], 0, v172, v172 op_sel_hi:[0,0,0]
	v_mfma_scale_f32_16x16x128_f8f6f4 v[110:113], v[18:25], v[222:229], 0, v172, v172 op_sel_hi:[0,0,0]
	v_mfma_scale_f32_16x16x128_f8f6f4 v[102:105], v[26:33], v[222:229], 0, v172, v172 op_sel_hi:[0,0,0]
	s_and_b64 s[24:25], s[24:25], exec
	v_mfma_scale_f32_16x16x128_f8f6f4 v[154:157], v[2:9], v[230:237], 0, v172, v172 op_sel_hi:[0,0,0]
	v_mfma_scale_f32_16x16x128_f8f6f4 v[146:149], v[10:17], v[230:237], 0, v172, v172 op_sel_hi:[0,0,0]
	v_mfma_scale_f32_16x16x128_f8f6f4 v[138:141], v[2:9], v[238:245], 0, v172, v172 op_sel_hi:[0,0,0]
	v_mfma_scale_f32_16x16x128_f8f6f4 v[130:133], v[10:17], v[238:245], 0, v172, v172 op_sel_hi:[0,0,0]
	v_mfma_scale_f32_16x16x128_f8f6f4 v[122:125], v[2:9], v[246:253], 0, v172, v172 op_sel_hi:[0,0,0]
	v_mfma_scale_f32_16x16x128_f8f6f4 v[114:117], v[10:17], v[246:253], 0, v172, v172 op_sel_hi:[0,0,0]
	v_mfma_scale_f32_16x16x128_f8f6f4 v[106:109], v[2:9], v[222:229], 0, v172, v172 op_sel_hi:[0,0,0]
	v_mfma_scale_f32_16x16x128_f8f6f4 v[98:101], v[10:17], v[222:229], 0, v172, v172 op_sel_hi:[0,0,0]
	s_cselect_b32 s24, s53, s63
	s_barrier
	s_lshl_b32 s24, s24, 10
	s_add_i32 s24, s24, 0
	s_add_i32 s24, s24, 0x20800
	v_lshl_add_u32 v0, v170, 2, s24
	v_lshl_add_u32 v214, v171, 2, s24
	ds_read_b32 v166, v0
	ds_read_b32 v167, v214
	ds_read_b128 v[226:229], v191
	s_mov_b32 m0, s34
	s_add_u32 s24, s22, 0x20000
	s_waitcnt lgkmcnt(0)
	v_lshl_or_b32 v215, v166, 10, v173
	v_lshl_or_b32 v216, v167, 10, v173
	v_lshl_add_u64 v[166:167], s[22:23], 0, v[164:165]
	ds_read_b128 v[222:225], v211 offset:16384
	ds_read_b128 v[230:233], v211 offset:18432
	ds_read_b128 v[234:237], v192
	ds_read_b128 v[242:245], v193
	ds_read_b128 v[238:241], v211 offset:20480
	ds_read_b128 v[246:249], v211 offset:22528
	ds_read_b128 v[250:253], v194
	global_load_lds_dwordx4 v[166:167], off
	v_lshl_add_u64 v[168:169], s[22:23], 0, v[162:163]
	s_mov_b32 m0, s35
	s_addc_u32 s25, s23, 0
	global_load_lds_dwordx4 v[168:169], off
	v_lshl_add_u64 v[212:213], s[24:25], 0, v[164:165]
	s_mov_b32 m0, s36
	s_nop 0
	global_load_lds_dwordx4 v[212:213], off
	v_lshl_add_u64 v[212:213], s[24:25], 0, v[162:163]
	s_mov_b32 m0, s37
	s_nop 0
	global_load_lds_dwordx4 v[212:213], off
	s_mov_b32 m0, s31
	s_nop 0
	global_load_lds_dwordx4 v215, s[20:21]
	s_mov_b32 m0, s40
	s_nop 0
	global_load_lds_dwordx4 v216, s[20:21]
	s_waitcnt vmcnt(8)
	s_waitcnt lgkmcnt(0)
	s_barrier
	s_waitcnt lgkmcnt(0)
	v_mfma_scale_f32_16x16x128_f8f6f4 v[94:97], v[18:25], v[222:229], 0, v172, v172 op_sel_hi:[0,0,0]
	v_mfma_scale_f32_16x16x128_f8f6f4 v[86:89], v[26:33], v[222:229], 0, v172, v172 op_sel_hi:[0,0,0]
	v_mfma_scale_f32_16x16x128_f8f6f4 v[78:81], v[18:25], v[230:237], 0, v172, v172 op_sel_hi:[0,0,0]
	v_mfma_scale_f32_16x16x128_f8f6f4 v[70:73], v[26:33], v[230:237], 0, v172, v172 op_sel_hi:[0,0,0]
	v_mfma_scale_f32_16x16x128_f8f6f4 v[62:65], v[18:25], v[238:245], 0, v172, v172 op_sel_hi:[0,0,0]
	v_mfma_scale_f32_16x16x128_f8f6f4 v[54:57], v[26:33], v[238:245], 0, v172, v172 op_sel_hi:[0,0,0]
	v_mfma_scale_f32_16x16x128_f8f6f4 v[46:49], v[18:25], v[246:253], 0, v172, v172 op_sel_hi:[0,0,0]
	v_mfma_scale_f32_16x16x128_f8f6f4 v[38:41], v[26:33], v[246:253], 0, v172, v172 op_sel_hi:[0,0,0]
	v_mfma_scale_f32_16x16x128_f8f6f4 v[90:93], v[2:9], v[222:229], 0, v172, v172 op_sel_hi:[0,0,0]
	v_mfma_scale_f32_16x16x128_f8f6f4 v[82:85], v[10:17], v[222:229], 0, v172, v172 op_sel_hi:[0,0,0]
	v_mfma_scale_f32_16x16x128_f8f6f4 v[74:77], v[2:9], v[230:237], 0, v172, v172 op_sel_hi:[0,0,0]
	v_mfma_scale_f32_16x16x128_f8f6f4 v[66:69], v[10:17], v[230:237], 0, v172, v172 op_sel_hi:[0,0,0]
	v_mfma_scale_f32_16x16x128_f8f6f4 v[58:61], v[2:9], v[238:245], 0, v172, v172 op_sel_hi:[0,0,0]
	v_mfma_scale_f32_16x16x128_f8f6f4 v[50:53], v[10:17], v[238:245], 0, v172, v172 op_sel_hi:[0,0,0]
	v_mfma_scale_f32_16x16x128_f8f6f4 v[42:45], v[2:9], v[246:253], 0, v172, v172 op_sel_hi:[0,0,0]
	v_mfma_scale_f32_16x16x128_f8f6f4 v[34:37], v[10:17], v[246:253], 0, v172, v172 op_sel_hi:[0,0,0]
	s_barrier
	ds_read_b32 v2, v0 offset:512
	s_waitcnt lgkmcnt(0)
	v_lshl_or_b32 v212, v2, 10, v173
	ds_read_b32 v2, v214 offset:512
	s_waitcnt lgkmcnt(0)
	v_lshl_or_b32 v213, v2, 10, v173
	ds_read_b128 v[2:5], v179
	ds_read_b128 v[6:9], v195
	ds_read_b128 v[18:21], v180
	ds_read_b128 v[22:25], v196
	ds_read_b128 v[10:13], v181
	ds_read_b128 v[14:17], v197
	ds_read_b128 v[26:29], v182
	ds_read_b128 v[30:33], v198
	s_mov_b32 m0, s41
	ds_read_b128 v[222:225], v211 offset:32768
	ds_read_b128 v[230:233], v211 offset:34816
	ds_read_b128 v[226:229], v199
	ds_read_b128 v[234:237], v200
	ds_read_b128 v[238:241], v211 offset:36864
	ds_read_b128 v[246:249], v211 offset:38912
	ds_read_b128 v[242:245], v201
	ds_read_b128 v[250:253], v202
	global_load_lds_dwordx4 v212, s[20:21]
	s_mov_b32 m0, s42
	s_nop 0
	global_load_lds_dwordx4 v213, s[20:21]
	s_waitcnt vmcnt(8)
	s_waitcnt lgkmcnt(0)
	s_barrier
	s_waitcnt lgkmcnt(0)
	v_mfma_scale_f32_16x16x128_f8f6f4 v[158:161], v[2:9], v[222:229], v[158:161], v172, v172 op_sel_hi:[0,0,0]
	v_mfma_scale_f32_16x16x128_f8f6f4 v[150:153], v[18:25], v[222:229], v[150:153], v172, v172 op_sel_hi:[0,0,0]
	v_mfma_scale_f32_16x16x128_f8f6f4 v[142:145], v[2:9], v[230:237], v[142:145], v172, v172 op_sel_hi:[0,0,0]
	v_mfma_scale_f32_16x16x128_f8f6f4 v[134:137], v[18:25], v[230:237], v[134:137], v172, v172 op_sel_hi:[0,0,0]
	v_mfma_scale_f32_16x16x128_f8f6f4 v[126:129], v[2:9], v[238:245], v[126:129], v172, v172 op_sel_hi:[0,0,0]
	v_mfma_scale_f32_16x16x128_f8f6f4 v[118:121], v[18:25], v[238:245], v[118:121], v172, v172 op_sel_hi:[0,0,0]
	v_mfma_scale_f32_16x16x128_f8f6f4 v[110:113], v[2:9], v[246:253], v[110:113], v172, v172 op_sel_hi:[0,0,0]
	v_mfma_scale_f32_16x16x128_f8f6f4 v[102:105], v[18:25], v[246:253], v[102:105], v172, v172 op_sel_hi:[0,0,0]
	v_mfma_scale_f32_16x16x128_f8f6f4 v[154:157], v[10:17], v[222:229], v[154:157], v172, v172 op_sel_hi:[0,0,0]
	v_mfma_scale_f32_16x16x128_f8f6f4 v[146:149], v[26:33], v[222:229], v[146:149], v172, v172 op_sel_hi:[0,0,0]
	v_mfma_scale_f32_16x16x128_f8f6f4 v[138:141], v[10:17], v[230:237], v[138:141], v172, v172 op_sel_hi:[0,0,0]
	v_mfma_scale_f32_16x16x128_f8f6f4 v[130:133], v[26:33], v[230:237], v[130:133], v172, v172 op_sel_hi:[0,0,0]
	v_mfma_scale_f32_16x16x128_f8f6f4 v[122:125], v[10:17], v[238:245], v[122:125], v172, v172 op_sel_hi:[0,0,0]
	v_mfma_scale_f32_16x16x128_f8f6f4 v[114:117], v[26:33], v[238:245], v[114:117], v172, v172 op_sel_hi:[0,0,0]
	v_mfma_scale_f32_16x16x128_f8f6f4 v[106:109], v[10:17], v[246:253], v[106:109], v172, v172 op_sel_hi:[0,0,0]
	v_mfma_scale_f32_16x16x128_f8f6f4 v[98:101], v[26:33], v[246:253], v[98:101], v172, v172 op_sel_hi:[0,0,0]
	s_barrier
	s_mov_b32 m0, s43
	ds_read_b32 v0, v0
	ds_read_b32 v212, v214
	ds_read_b128 v[226:229], v203
	v_lshl_add_u64 v[166:167], v[166:167], 0, s[78:79]
	s_add_u32 s22, s22, 0x20080
	ds_read_b128 v[222:225], v211 offset:49152
	ds_read_b128 v[230:233], v211 offset:51200
	ds_read_b128 v[234:237], v206
	ds_read_b128 v[242:245], v207
	ds_read_b128 v[238:241], v211 offset:53248
	ds_read_b128 v[246:249], v211 offset:55296
	ds_read_b128 v[250:253], v208
	global_load_lds_dwordx4 v[166:167], off
	v_lshl_add_u64 v[166:167], v[168:169], 0, s[78:79]
	s_mov_b32 m0, s44
	s_addc_u32 s23, s23, 0
	global_load_lds_dwordx4 v[166:167], off
	v_lshl_add_u64 v[166:167], s[22:23], 0, v[164:165]
	s_mov_b32 m0, s51
	s_waitcnt lgkmcnt(0)
	v_lshl_or_b32 v0, v0, 10, v173
	global_load_lds_dwordx4 v[166:167], off
	v_lshl_add_u64 v[166:167], s[22:23], 0, v[162:163]
	s_mov_b32 m0, s52
	v_lshl_or_b32 v212, v212, 10, v173
	global_load_lds_dwordx4 v[166:167], off
	v_lshl_add_u64 v[166:167], s[20:21], 0, v[0:1]
	v_lshl_add_u64 v[166:167], v[166:167], 0, s[78:79]
	s_mov_b32 m0, s45
	v_mov_b32_e32 v213, v1
	global_load_lds_dwordx4 v[166:167], off
	v_lshl_add_u64 v[166:167], s[20:21], 0, v[212:213]
	v_lshl_add_u64 v[166:167], v[166:167], 0, s[78:79]
	s_mov_b32 m0, s48
	s_nop 0
	global_load_lds_dwordx4 v[166:167], off
	s_waitcnt vmcnt(8)
	s_waitcnt lgkmcnt(0)
	s_barrier
	v_mfma_scale_f32_16x16x128_f8f6f4 v[94:97], v[2:9], v[222:229], v[94:97], v172, v172 op_sel_hi:[0,0,0]
	v_mfma_scale_f32_16x16x128_f8f6f4 v[86:89], v[18:25], v[222:229], v[86:89], v172, v172 op_sel_hi:[0,0,0]
	v_mfma_scale_f32_16x16x128_f8f6f4 v[78:81], v[2:9], v[230:237], v[78:81], v172, v172 op_sel_hi:[0,0,0]
	v_mfma_scale_f32_16x16x128_f8f6f4 v[70:73], v[18:25], v[230:237], v[70:73], v172, v172 op_sel_hi:[0,0,0]
	v_mfma_scale_f32_16x16x128_f8f6f4 v[62:65], v[2:9], v[238:245], v[62:65], v172, v172 op_sel_hi:[0,0,0]
	v_mfma_scale_f32_16x16x128_f8f6f4 v[54:57], v[18:25], v[238:245], v[54:57], v172, v172 op_sel_hi:[0,0,0]
	v_mfma_scale_f32_16x16x128_f8f6f4 v[46:49], v[2:9], v[246:253], v[46:49], v172, v172 op_sel_hi:[0,0,0]
	v_mfma_scale_f32_16x16x128_f8f6f4 v[38:41], v[18:25], v[246:253], v[38:41], v172, v172 op_sel_hi:[0,0,0]
	v_mfma_scale_f32_16x16x128_f8f6f4 v[90:93], v[10:17], v[222:229], v[90:93], v172, v172 op_sel_hi:[0,0,0]
	v_mfma_scale_f32_16x16x128_f8f6f4 v[82:85], v[26:33], v[222:229], v[82:85], v172, v172 op_sel_hi:[0,0,0]
	v_mfma_scale_f32_16x16x128_f8f6f4 v[74:77], v[10:17], v[230:237], v[74:77], v172, v172 op_sel_hi:[0,0,0]
	v_mfma_scale_f32_16x16x128_f8f6f4 v[66:69], v[26:33], v[230:237], v[66:69], v172, v172 op_sel_hi:[0,0,0]
	v_mfma_scale_f32_16x16x128_f8f6f4 v[58:61], v[10:17], v[238:245], v[58:61], v172, v172 op_sel_hi:[0,0,0]
	v_mfma_scale_f32_16x16x128_f8f6f4 v[50:53], v[26:33], v[238:245], v[50:53], v172, v172 op_sel_hi:[0,0,0]
	v_mfma_scale_f32_16x16x128_f8f6f4 v[42:45], v[10:17], v[246:253], v[42:45], v172, v172 op_sel_hi:[0,0,0]
	v_mfma_scale_f32_16x16x128_f8f6f4 v[34:37], v[26:33], v[246:253], v[34:37], v172, v172 op_sel_hi:[0,0,0]
	s_barrier
	s_add_i32 s70, s70, 2
	s_add_u32 s18, s18, 0x100
	s_addc_u32 s19, s19, 0
	s_add_u32 s68, s68, 0x100
	s_addc_u32 s69, s69, 0
	s_cmp_gt_u32 s70, 5
.LBB0_1788:
	ds_read_b32 v0, v209 offset:512
	ds_read_b32 v166, v210 offset:512
	ds_read_b128 v[22:25], v186
	ds_read_b128 v[18:21], v175
	ds_read_b128 v[26:29], v176
	ds_read_b128 v[30:33], v187
	ds_read_b128 v[6:9], v188
	ds_read_b128 v[2:5], v177
	ds_read_b128 v[10:13], v178
	ds_read_b128 v[14:17], v189
	s_add_u32 s22, s18, 0x80
	s_addc_u32 s23, s19, 0
	s_cmp_eq_u32 s70, 4
	s_cselect_b64 s[24:25], -1, 0
	s_and_b64 s[20:21], s[24:25], exec
	s_cselect_b32 s21, s5, s23
	s_cselect_b32 s20, s4, s22
	s_cselect_b32 s22, s14, s68
	s_cselect_b32 s23, s15, s69
	s_and_b64 s[24:25], s[16:17], s[24:25]
	v_add_u32_e32 v211, 0, v174
	s_waitcnt lgkmcnt(0)
	v_lshl_or_b32 v0, v0, 10, v173
	s_add_i32 m0, s31, 0xc000
	ds_read_b128 v[230:233], v211
	ds_read_b128 v[238:241], v211 offset:2048
	ds_read_b128 v[234:237], v190
	ds_read_b128 v[242:245], v190 offset:2048
	ds_read_b128 v[246:249], v211 offset:4096
	ds_read_b128 v[222:225], v211 offset:6144
	ds_read_b128 v[250:253], v190 offset:4096
	ds_read_b128 v[226:229], v190 offset:6144
	global_load_lds_dwordx4 v0, s[18:19]
	v_lshl_or_b32 v0, v166, 10, v173
	s_add_i32 m0, s31, 0xe000
	s_nop 0
	global_load_lds_dwordx4 v0, s[18:19]
	s_waitcnt vmcnt(8)
	s_waitcnt lgkmcnt(0)
	s_barrier
	s_waitcnt lgkmcnt(0)
	v_mfma_scale_f32_16x16x128_f8f6f4 v[158:161], v[18:25], v[230:237], v[158:161], v172, v172 op_sel_hi:[0,0,0]
	v_mfma_scale_f32_16x16x128_f8f6f4 v[150:153], v[26:33], v[230:237], v[150:153], v172, v172 op_sel_hi:[0,0,0]
	v_mfma_scale_f32_16x16x128_f8f6f4 v[142:145], v[18:25], v[238:245], v[142:145], v172, v172 op_sel_hi:[0,0,0]
	v_mfma_scale_f32_16x16x128_f8f6f4 v[134:137], v[26:33], v[238:245], v[134:137], v172, v172 op_sel_hi:[0,0,0]
	v_mfma_scale_f32_16x16x128_f8f6f4 v[126:129], v[18:25], v[246:253], v[126:129], v172, v172 op_sel_hi:[0,0,0]
	v_mfma_scale_f32_16x16x128_f8f6f4 v[118:121], v[26:33], v[246:253], v[118:121], v172, v172 op_sel_hi:[0,0,0]
	v_mfma_scale_f32_16x16x128_f8f6f4 v[110:113], v[18:25], v[222:229], v[110:113], v172, v172 op_sel_hi:[0,0,0]
	v_mfma_scale_f32_16x16x128_f8f6f4 v[102:105], v[26:33], v[222:229], v[102:105], v172, v172 op_sel_hi:[0,0,0]
	s_and_b64 s[24:25], s[24:25], exec
	v_mfma_scale_f32_16x16x128_f8f6f4 v[154:157], v[2:9], v[230:237], v[154:157], v172, v172 op_sel_hi:[0,0,0]
	v_mfma_scale_f32_16x16x128_f8f6f4 v[146:149], v[10:17], v[230:237], v[146:149], v172, v172 op_sel_hi:[0,0,0]
	v_mfma_scale_f32_16x16x128_f8f6f4 v[138:141], v[2:9], v[238:245], v[138:141], v172, v172 op_sel_hi:[0,0,0]
	v_mfma_scale_f32_16x16x128_f8f6f4 v[130:133], v[10:17], v[238:245], v[130:133], v172, v172 op_sel_hi:[0,0,0]
	v_mfma_scale_f32_16x16x128_f8f6f4 v[122:125], v[2:9], v[246:253], v[122:125], v172, v172 op_sel_hi:[0,0,0]
	v_mfma_scale_f32_16x16x128_f8f6f4 v[114:117], v[10:17], v[246:253], v[114:117], v172, v172 op_sel_hi:[0,0,0]
	v_mfma_scale_f32_16x16x128_f8f6f4 v[106:109], v[2:9], v[222:229], v[106:109], v172, v172 op_sel_hi:[0,0,0]
	v_mfma_scale_f32_16x16x128_f8f6f4 v[98:101], v[10:17], v[222:229], v[98:101], v172, v172 op_sel_hi:[0,0,0]
	s_cselect_b32 s24, s53, s63
	s_barrier
	s_lshl_b32 s24, s24, 10
	s_add_i32 s24, s24, 0
	s_add_i32 s24, s24, 0x20800
	v_lshl_add_u32 v0, v170, 2, s24
	v_lshl_add_u32 v214, v171, 2, s24
	ds_read_b32 v166, v0
	ds_read_b32 v167, v214
	ds_read_b128 v[226:229], v191
	s_mov_b32 m0, s34
	s_add_u32 s24, s22, 0x20000
	s_waitcnt lgkmcnt(0)
	v_lshl_or_b32 v215, v166, 10, v173
	v_lshl_or_b32 v216, v167, 10, v173
	v_lshl_add_u64 v[166:167], s[22:23], 0, v[164:165]
	ds_read_b128 v[222:225], v211 offset:16384
	ds_read_b128 v[230:233], v211 offset:18432
	ds_read_b128 v[234:237], v192
	ds_read_b128 v[242:245], v193
	ds_read_b128 v[238:241], v211 offset:20480
	ds_read_b128 v[246:249], v211 offset:22528
	ds_read_b128 v[250:253], v194
	global_load_lds_dwordx4 v[166:167], off
	v_lshl_add_u64 v[168:169], s[22:23], 0, v[162:163]
	s_mov_b32 m0, s35
	s_addc_u32 s25, s23, 0
	global_load_lds_dwordx4 v[168:169], off
	v_lshl_add_u64 v[212:213], s[24:25], 0, v[164:165]
	s_mov_b32 m0, s36
	s_nop 0
	global_load_lds_dwordx4 v[212:213], off
	v_lshl_add_u64 v[212:213], s[24:25], 0, v[162:163]
	s_mov_b32 m0, s37
	s_nop 0
	global_load_lds_dwordx4 v[212:213], off
	s_mov_b32 m0, s31
	s_nop 0
	global_load_lds_dwordx4 v215, s[20:21]
	s_mov_b32 m0, s40
	s_nop 0
	global_load_lds_dwordx4 v216, s[20:21]
	s_waitcnt vmcnt(8)
	s_waitcnt lgkmcnt(0)
	s_barrier
	s_waitcnt lgkmcnt(0)
	v_mfma_scale_f32_16x16x128_f8f6f4 v[94:97], v[18:25], v[222:229], v[94:97], v172, v172 op_sel_hi:[0,0,0]
	v_mfma_scale_f32_16x16x128_f8f6f4 v[86:89], v[26:33], v[222:229], v[86:89], v172, v172 op_sel_hi:[0,0,0]
	v_mfma_scale_f32_16x16x128_f8f6f4 v[78:81], v[18:25], v[230:237], v[78:81], v172, v172 op_sel_hi:[0,0,0]
	v_mfma_scale_f32_16x16x128_f8f6f4 v[70:73], v[26:33], v[230:237], v[70:73], v172, v172 op_sel_hi:[0,0,0]
	v_mfma_scale_f32_16x16x128_f8f6f4 v[62:65], v[18:25], v[238:245], v[62:65], v172, v172 op_sel_hi:[0,0,0]
	v_mfma_scale_f32_16x16x128_f8f6f4 v[54:57], v[26:33], v[238:245], v[54:57], v172, v172 op_sel_hi:[0,0,0]
	v_mfma_scale_f32_16x16x128_f8f6f4 v[46:49], v[18:25], v[246:253], v[46:49], v172, v172 op_sel_hi:[0,0,0]
	v_mfma_scale_f32_16x16x128_f8f6f4 v[38:41], v[26:33], v[246:253], v[38:41], v172, v172 op_sel_hi:[0,0,0]
	v_mfma_scale_f32_16x16x128_f8f6f4 v[90:93], v[2:9], v[222:229], v[90:93], v172, v172 op_sel_hi:[0,0,0]
	v_mfma_scale_f32_16x16x128_f8f6f4 v[82:85], v[10:17], v[222:229], v[82:85], v172, v172 op_sel_hi:[0,0,0]
	v_mfma_scale_f32_16x16x128_f8f6f4 v[74:77], v[2:9], v[230:237], v[74:77], v172, v172 op_sel_hi:[0,0,0]
	v_mfma_scale_f32_16x16x128_f8f6f4 v[66:69], v[10:17], v[230:237], v[66:69], v172, v172 op_sel_hi:[0,0,0]
	v_mfma_scale_f32_16x16x128_f8f6f4 v[58:61], v[2:9], v[238:245], v[58:61], v172, v172 op_sel_hi:[0,0,0]
	v_mfma_scale_f32_16x16x128_f8f6f4 v[50:53], v[10:17], v[238:245], v[50:53], v172, v172 op_sel_hi:[0,0,0]
	v_mfma_scale_f32_16x16x128_f8f6f4 v[42:45], v[2:9], v[246:253], v[42:45], v172, v172 op_sel_hi:[0,0,0]
	v_mfma_scale_f32_16x16x128_f8f6f4 v[34:37], v[10:17], v[246:253], v[34:37], v172, v172 op_sel_hi:[0,0,0]
	s_barrier
	ds_read_b32 v2, v0 offset:512
	s_waitcnt lgkmcnt(0)
	v_lshl_or_b32 v212, v2, 10, v173
	ds_read_b32 v2, v214 offset:512
	s_waitcnt lgkmcnt(0)
	v_lshl_or_b32 v213, v2, 10, v173
	ds_read_b128 v[2:5], v179
	ds_read_b128 v[6:9], v195
	ds_read_b128 v[18:21], v180
	ds_read_b128 v[22:25], v196
	ds_read_b128 v[10:13], v181
	ds_read_b128 v[14:17], v197
	ds_read_b128 v[26:29], v182
	ds_read_b128 v[30:33], v198
	s_mov_b32 m0, s41
	ds_read_b128 v[222:225], v211 offset:32768
	ds_read_b128 v[230:233], v211 offset:34816
	ds_read_b128 v[226:229], v199
	ds_read_b128 v[234:237], v200
	ds_read_b128 v[238:241], v211 offset:36864
	ds_read_b128 v[246:249], v211 offset:38912
	ds_read_b128 v[242:245], v201
	ds_read_b128 v[250:253], v202
	global_load_lds_dwordx4 v212, s[20:21]
	s_mov_b32 m0, s42
	s_nop 0
	global_load_lds_dwordx4 v213, s[20:21]
	s_waitcnt vmcnt(8)
	s_waitcnt lgkmcnt(0)
	s_barrier
	s_waitcnt lgkmcnt(0)
	v_mfma_scale_f32_16x16x128_f8f6f4 v[158:161], v[2:9], v[222:229], v[158:161], v172, v172 op_sel_hi:[0,0,0]
	v_mfma_scale_f32_16x16x128_f8f6f4 v[150:153], v[18:25], v[222:229], v[150:153], v172, v172 op_sel_hi:[0,0,0]
	v_mfma_scale_f32_16x16x128_f8f6f4 v[142:145], v[2:9], v[230:237], v[142:145], v172, v172 op_sel_hi:[0,0,0]
	v_mfma_scale_f32_16x16x128_f8f6f4 v[134:137], v[18:25], v[230:237], v[134:137], v172, v172 op_sel_hi:[0,0,0]
	v_mfma_scale_f32_16x16x128_f8f6f4 v[126:129], v[2:9], v[238:245], v[126:129], v172, v172 op_sel_hi:[0,0,0]
	v_mfma_scale_f32_16x16x128_f8f6f4 v[118:121], v[18:25], v[238:245], v[118:121], v172, v172 op_sel_hi:[0,0,0]
	v_mfma_scale_f32_16x16x128_f8f6f4 v[110:113], v[2:9], v[246:253], v[110:113], v172, v172 op_sel_hi:[0,0,0]
	v_mfma_scale_f32_16x16x128_f8f6f4 v[102:105], v[18:25], v[246:253], v[102:105], v172, v172 op_sel_hi:[0,0,0]
	v_mfma_scale_f32_16x16x128_f8f6f4 v[154:157], v[10:17], v[222:229], v[154:157], v172, v172 op_sel_hi:[0,0,0]
	v_mfma_scale_f32_16x16x128_f8f6f4 v[146:149], v[26:33], v[222:229], v[146:149], v172, v172 op_sel_hi:[0,0,0]
	v_mfma_scale_f32_16x16x128_f8f6f4 v[138:141], v[10:17], v[230:237], v[138:141], v172, v172 op_sel_hi:[0,0,0]
	v_mfma_scale_f32_16x16x128_f8f6f4 v[130:133], v[26:33], v[230:237], v[130:133], v172, v172 op_sel_hi:[0,0,0]
	v_mfma_scale_f32_16x16x128_f8f6f4 v[122:125], v[10:17], v[238:245], v[122:125], v172, v172 op_sel_hi:[0,0,0]
	v_mfma_scale_f32_16x16x128_f8f6f4 v[114:117], v[26:33], v[238:245], v[114:117], v172, v172 op_sel_hi:[0,0,0]
	v_mfma_scale_f32_16x16x128_f8f6f4 v[106:109], v[10:17], v[246:253], v[106:109], v172, v172 op_sel_hi:[0,0,0]
	v_mfma_scale_f32_16x16x128_f8f6f4 v[98:101], v[26:33], v[246:253], v[98:101], v172, v172 op_sel_hi:[0,0,0]
	s_barrier
	s_mov_b32 m0, s43
	ds_read_b32 v0, v0
	ds_read_b32 v212, v214
	ds_read_b128 v[226:229], v203
	v_lshl_add_u64 v[166:167], v[166:167], 0, s[78:79]
	s_add_u32 s22, s22, 0x20080
	ds_read_b128 v[222:225], v211 offset:49152
	ds_read_b128 v[230:233], v211 offset:51200
	ds_read_b128 v[234:237], v206
	ds_read_b128 v[242:245], v207
	ds_read_b128 v[238:241], v211 offset:53248
	ds_read_b128 v[246:249], v211 offset:55296
	ds_read_b128 v[250:253], v208
	global_load_lds_dwordx4 v[166:167], off
	v_lshl_add_u64 v[166:167], v[168:169], 0, s[78:79]
	s_mov_b32 m0, s44
	s_addc_u32 s23, s23, 0
	global_load_lds_dwordx4 v[166:167], off
	v_lshl_add_u64 v[166:167], s[22:23], 0, v[164:165]
	s_mov_b32 m0, s51
	s_waitcnt lgkmcnt(0)
	v_lshl_or_b32 v0, v0, 10, v173
	global_load_lds_dwordx4 v[166:167], off
	v_lshl_add_u64 v[166:167], s[22:23], 0, v[162:163]
	s_mov_b32 m0, s52
	v_lshl_or_b32 v212, v212, 10, v173
	global_load_lds_dwordx4 v[166:167], off
	v_lshl_add_u64 v[166:167], s[20:21], 0, v[0:1]
	v_lshl_add_u64 v[166:167], v[166:167], 0, s[78:79]
	s_mov_b32 m0, s45
	v_mov_b32_e32 v213, v1
	global_load_lds_dwordx4 v[166:167], off
	v_lshl_add_u64 v[166:167], s[20:21], 0, v[212:213]
	v_lshl_add_u64 v[166:167], v[166:167], 0, s[78:79]
	s_mov_b32 m0, s48
	s_nop 0
	global_load_lds_dwordx4 v[166:167], off
	s_waitcnt vmcnt(8)
	s_waitcnt lgkmcnt(0)
	s_barrier
	v_mfma_scale_f32_16x16x128_f8f6f4 v[94:97], v[2:9], v[222:229], v[94:97], v172, v172 op_sel_hi:[0,0,0]
	v_mfma_scale_f32_16x16x128_f8f6f4 v[86:89], v[18:25], v[222:229], v[86:89], v172, v172 op_sel_hi:[0,0,0]
	v_mfma_scale_f32_16x16x128_f8f6f4 v[78:81], v[2:9], v[230:237], v[78:81], v172, v172 op_sel_hi:[0,0,0]
	v_mfma_scale_f32_16x16x128_f8f6f4 v[70:73], v[18:25], v[230:237], v[70:73], v172, v172 op_sel_hi:[0,0,0]
	v_mfma_scale_f32_16x16x128_f8f6f4 v[62:65], v[2:9], v[238:245], v[62:65], v172, v172 op_sel_hi:[0,0,0]
	v_mfma_scale_f32_16x16x128_f8f6f4 v[54:57], v[18:25], v[238:245], v[54:57], v172, v172 op_sel_hi:[0,0,0]
	v_mfma_scale_f32_16x16x128_f8f6f4 v[46:49], v[2:9], v[246:253], v[46:49], v172, v172 op_sel_hi:[0,0,0]
	v_mfma_scale_f32_16x16x128_f8f6f4 v[38:41], v[18:25], v[246:253], v[38:41], v172, v172 op_sel_hi:[0,0,0]
	v_mfma_scale_f32_16x16x128_f8f6f4 v[90:93], v[10:17], v[222:229], v[90:93], v172, v172 op_sel_hi:[0,0,0]
	v_mfma_scale_f32_16x16x128_f8f6f4 v[82:85], v[26:33], v[222:229], v[82:85], v172, v172 op_sel_hi:[0,0,0]
	v_mfma_scale_f32_16x16x128_f8f6f4 v[74:77], v[10:17], v[230:237], v[74:77], v172, v172 op_sel_hi:[0,0,0]
	v_mfma_scale_f32_16x16x128_f8f6f4 v[66:69], v[26:33], v[230:237], v[66:69], v172, v172 op_sel_hi:[0,0,0]
	v_mfma_scale_f32_16x16x128_f8f6f4 v[58:61], v[10:17], v[238:245], v[58:61], v172, v172 op_sel_hi:[0,0,0]
	v_mfma_scale_f32_16x16x128_f8f6f4 v[50:53], v[26:33], v[238:245], v[50:53], v172, v172 op_sel_hi:[0,0,0]
	v_mfma_scale_f32_16x16x128_f8f6f4 v[42:45], v[10:17], v[246:253], v[42:45], v172, v172 op_sel_hi:[0,0,0]
	v_mfma_scale_f32_16x16x128_f8f6f4 v[34:37], v[26:33], v[246:253], v[34:37], v172, v172 op_sel_hi:[0,0,0]
	s_barrier
	s_add_i32 s70, s70, 2
	s_add_u32 s18, s18, 0x100
	s_addc_u32 s19, s19, 0
	s_add_u32 s68, s68, 0x100
	s_addc_u32 s69, s69, 0
	s_cmp_gt_u32 s70, 5
	s_cbranch_scc0 .LBB0_1788
	s_nop 15
	s_nop 7
	s_and_b64 vcc, exec, s[12:13]
	s_cbranch_vccz .LBB0_1791
	s_barrier

.LBB0_1851:
	s_setprio 0
	s_mul_i32 s4, s73, 10
	s_add_i32 s26, s4, 10
	s_movk_i32 s4, 0x48
	s_ashr_i32 s5, s4, 31
	s_lshl_b64 s[4:5], s[4:5], 2
	s_add_u32 s4, s0, s4
	s_addc_u32 s5, s1, s5
	s_load_dwordx2 s[6:7], s[4:5], 0x0
	s_waitcnt lgkmcnt(0)
	s_cmp_le_i32 s6, s26
	s_cselect_b64 s[4:5], -1, 0
	s_cmp_lt_i32 s26, s7
	s_cselect_b64 s[6:7], -1, 0
	s_and_b64 s[4:5], s[4:5], s[6:7]
	s_andn2_b64 vcc, exec, s[4:5]
	s_cbranch_vccz .LBB0_1852
	s_getpc_b64 s[98:99]

.LBB0_1864:
	s_cmp_lg_u32 s13, 1
	s_cbranch_scc1 .Lmoe2_prio_skip
	s_setprio 1

.LBB0_1871:
	s_add_u32 s13, s20, 0x100
	s_addc_u32 s49, s21, 0
	s_mov_b32 s68, -2
	ds_read_b128 v[18:21], v182
	ds_read_b128 v[26:29], v183
	ds_read_b128 v[22:25], v193
	ds_read_b128 v[30:33], v194
	ds_read_b128 v[2:5], v184
	ds_read_b128 v[10:13], v185
	ds_read_b128 v[6:9], v195
	ds_read_b128 v[14:17], v196
	s_add_u32 s20, s18, 0x100
	s_addc_u32 s21, s19, 0
	s_cmp_eq_u32 s68, 4
	s_cselect_b32 s25, s15, s21
	s_cselect_b32 s24, s14, s20
	s_cselect_b32 s23, s17, s49
	s_cselect_b32 s22, s16, s13
	v_add_u32_e32 v234, 0, v181
	v_lshl_add_u64 v[212:213], s[18:19], 0, v[168:169]
	s_add_i32 m0, s36, 0xc000
	ds_read_b128 v[172:175], v234
	ds_read_b128 v[222:225], v234 offset:2048
	ds_read_b128 v[176:179], v197
	ds_read_b128 v[226:229], v197 offset:2048
	ds_read_b128 v[236:239], v234 offset:4096
	ds_read_b128 v[244:247], v234 offset:6144
	ds_read_b128 v[240:243], v197 offset:4096
	ds_read_b128 v[248:251], v197 offset:6144
	global_load_lds_dwordx4 v[212:213], off
	v_lshl_add_u64 v[212:213], s[18:19], 0, v[170:171]
	s_add_i32 m0, s36, 0xe000
	s_nop 0
	global_load_lds_dwordx4 v[212:213], off
	s_waitcnt vmcnt(8)
	s_waitcnt lgkmcnt(0)
	s_barrier
	s_waitcnt lgkmcnt(0)
	v_mfma_scale_f32_16x16x128_f8f6f4 v[158:161], v[18:25], v[172:179], 0, v180, v180 op_sel_hi:[0,0,0]
	v_mfma_scale_f32_16x16x128_f8f6f4 v[154:157], v[26:33], v[172:179], 0, v180, v180 op_sel_hi:[0,0,0]
	v_mfma_scale_f32_16x16x128_f8f6f4 v[150:153], v[18:25], v[222:229], 0, v180, v180 op_sel_hi:[0,0,0]
	v_mfma_scale_f32_16x16x128_f8f6f4 v[146:149], v[26:33], v[222:229], 0, v180, v180 op_sel_hi:[0,0,0]
	v_mfma_scale_f32_16x16x128_f8f6f4 v[126:129], v[18:25], v[236:243], 0, v180, v180 op_sel_hi:[0,0,0]
	v_mfma_scale_f32_16x16x128_f8f6f4 v[122:125], v[26:33], v[236:243], 0, v180, v180 op_sel_hi:[0,0,0]
	v_mfma_scale_f32_16x16x128_f8f6f4 v[118:121], v[18:25], v[244:251], 0, v180, v180 op_sel_hi:[0,0,0]
	v_mfma_scale_f32_16x16x128_f8f6f4 v[114:117], v[26:33], v[244:251], 0, v180, v180 op_sel_hi:[0,0,0]
	v_mfma_scale_f32_16x16x128_f8f6f4 v[142:145], v[2:9], v[172:179], 0, v180, v180 op_sel_hi:[0,0,0]
	v_mfma_scale_f32_16x16x128_f8f6f4 v[138:141], v[10:17], v[172:179], 0, v180, v180 op_sel_hi:[0,0,0]
	v_mfma_scale_f32_16x16x128_f8f6f4 v[134:137], v[2:9], v[222:229], 0, v180, v180 op_sel_hi:[0,0,0]
	v_mfma_scale_f32_16x16x128_f8f6f4 v[130:133], v[10:17], v[222:229], 0, v180, v180 op_sel_hi:[0,0,0]
	v_mfma_scale_f32_16x16x128_f8f6f4 v[110:113], v[2:9], v[236:243], 0, v180, v180 op_sel_hi:[0,0,0]
	v_mfma_scale_f32_16x16x128_f8f6f4 v[106:109], v[10:17], v[236:243], 0, v180, v180 op_sel_hi:[0,0,0]
	v_mfma_scale_f32_16x16x128_f8f6f4 v[102:105], v[2:9], v[244:251], 0, v180, v180 op_sel_hi:[0,0,0]
	v_mfma_scale_f32_16x16x128_f8f6f4 v[98:101], v[10:17], v[244:251], 0, v180, v180 op_sel_hi:[0,0,0]
	s_barrier
	s_mov_b32 m0, s37
	v_lshl_add_u64 v[172:173], s[22:23], 0, v[0:1]
	s_add_u32 s18, s22, 0x20000
	ds_read_b128 v[222:225], v234 offset:16384
	ds_read_b128 v[236:239], v234 offset:18432
	ds_read_b128 v[226:229], v198
	ds_read_b128 v[240:243], v199
	ds_read_b128 v[244:247], v234 offset:20480
	ds_read_b128 v[212:215], v234 offset:22528
	ds_read_b128 v[248:251], v200
	ds_read_b128 v[216:219], v201
	global_load_lds_dwordx4 v[172:173], off
	v_lshl_add_u64 v[174:175], s[22:23], 0, v[162:163]
	s_mov_b32 m0, s40
	s_addc_u32 s19, s23, 0
	global_load_lds_dwordx4 v[174:175], off
	v_lshl_add_u64 v[176:177], s[18:19], 0, v[0:1]
	s_mov_b32 m0, s41
	v_lshl_add_u64 v[178:179], s[24:25], 0, v[166:167]
	global_load_lds_dwordx4 v[176:177], off
	v_lshl_add_u64 v[176:177], s[18:19], 0, v[162:163]
	s_mov_b32 m0, s42
	s_nop 0
	global_load_lds_dwordx4 v[176:177], off
	v_lshl_add_u64 v[176:177], s[24:25], 0, v[164:165]
	s_mov_b32 m0, s36
	s_nop 0
	global_load_lds_dwordx4 v[176:177], off
	s_mov_b32 m0, s43
	s_nop 0
	global_load_lds_dwordx4 v[178:179], off
	s_waitcnt vmcnt(8)
	s_waitcnt lgkmcnt(0)
	s_barrier
	s_waitcnt lgkmcnt(0)
	v_mfma_scale_f32_16x16x128_f8f6f4 v[94:97], v[18:25], v[222:229], 0, v180, v180 op_sel_hi:[0,0,0]
	v_mfma_scale_f32_16x16x128_f8f6f4 v[90:93], v[26:33], v[222:229], 0, v180, v180 op_sel_hi:[0,0,0]
	v_mfma_scale_f32_16x16x128_f8f6f4 v[86:89], v[18:25], v[236:243], 0, v180, v180 op_sel_hi:[0,0,0]
	v_mfma_scale_f32_16x16x128_f8f6f4 v[82:85], v[26:33], v[236:243], 0, v180, v180 op_sel_hi:[0,0,0]
	v_mfma_scale_f32_16x16x128_f8f6f4 v[62:65], v[18:25], v[244:251], 0, v180, v180 op_sel_hi:[0,0,0]
	v_mfma_scale_f32_16x16x128_f8f6f4 v[58:61], v[26:33], v[244:251], 0, v180, v180 op_sel_hi:[0,0,0]
	v_mfma_scale_f32_16x16x128_f8f6f4 v[54:57], v[18:25], v[212:219], 0, v180, v180 op_sel_hi:[0,0,0]
	v_mfma_scale_f32_16x16x128_f8f6f4 v[50:53], v[26:33], v[212:219], 0, v180, v180 op_sel_hi:[0,0,0]
	v_mfma_scale_f32_16x16x128_f8f6f4 v[78:81], v[2:9], v[222:229], 0, v180, v180 op_sel_hi:[0,0,0]
	v_mfma_scale_f32_16x16x128_f8f6f4 v[74:77], v[10:17], v[222:229], 0, v180, v180 op_sel_hi:[0,0,0]
	v_mfma_scale_f32_16x16x128_f8f6f4 v[70:73], v[2:9], v[236:243], 0, v180, v180 op_sel_hi:[0,0,0]
	v_mfma_scale_f32_16x16x128_f8f6f4 v[66:69], v[10:17], v[236:243], 0, v180, v180 op_sel_hi:[0,0,0]
	v_mfma_scale_f32_16x16x128_f8f6f4 v[46:49], v[2:9], v[244:251], 0, v180, v180 op_sel_hi:[0,0,0]
	v_mfma_scale_f32_16x16x128_f8f6f4 v[42:45], v[10:17], v[244:251], 0, v180, v180 op_sel_hi:[0,0,0]
	v_mfma_scale_f32_16x16x128_f8f6f4 v[38:41], v[2:9], v[212:219], 0, v180, v180 op_sel_hi:[0,0,0]
	v_mfma_scale_f32_16x16x128_f8f6f4 v[34:37], v[10:17], v[212:219], 0, v180, v180 op_sel_hi:[0,0,0]
	s_barrier
	ds_read_b128 v[2:5], v186
	ds_read_b128 v[10:13], v187
	ds_read_b128 v[6:9], v202
	ds_read_b128 v[14:17], v203
	ds_read_b128 v[18:21], v188
	ds_read_b128 v[26:29], v189
	ds_read_b128 v[22:25], v206
	ds_read_b128 v[30:33], v207
	s_add_u32 s18, s24, 0x20000
	s_addc_u32 s19, s25, 0
	s_mov_b32 m0, s44
	v_lshl_add_u64 v[252:253], s[18:19], 0, v[164:165]
	ds_read_b128 v[212:215], v234 offset:32768
	ds_read_b128 v[222:225], v234 offset:34816
	ds_read_b128 v[216:219], v208
	ds_read_b128 v[226:229], v209
	ds_read_b128 v[236:239], v234 offset:36864
	ds_read_b128 v[244:247], v234 offset:38912
	ds_read_b128 v[240:243], v210
	ds_read_b128 v[248:251], v211
	global_load_lds_dwordx4 v[252:253], off
	v_lshl_add_u64 v[252:253], s[18:19], 0, v[166:167]
	s_mov_b32 m0, s45
	s_nop 0
	global_load_lds_dwordx4 v[252:253], off
	s_waitcnt vmcnt(8)
	s_waitcnt lgkmcnt(0)
	s_barrier
	s_waitcnt lgkmcnt(0)
	v_mfma_scale_f32_16x16x128_f8f6f4 v[158:161], v[2:9], v[212:219], v[158:161], v180, v180 op_sel_hi:[0,0,0]
	v_mfma_scale_f32_16x16x128_f8f6f4 v[154:157], v[10:17], v[212:219], v[154:157], v180, v180 op_sel_hi:[0,0,0]
	v_mfma_scale_f32_16x16x128_f8f6f4 v[150:153], v[2:9], v[222:229], v[150:153], v180, v180 op_sel_hi:[0,0,0]
	v_mfma_scale_f32_16x16x128_f8f6f4 v[146:149], v[10:17], v[222:229], v[146:149], v180, v180 op_sel_hi:[0,0,0]
	v_mfma_scale_f32_16x16x128_f8f6f4 v[126:129], v[2:9], v[236:243], v[126:129], v180, v180 op_sel_hi:[0,0,0]
	v_mfma_scale_f32_16x16x128_f8f6f4 v[122:125], v[10:17], v[236:243], v[122:125], v180, v180 op_sel_hi:[0,0,0]
	v_mfma_scale_f32_16x16x128_f8f6f4 v[118:121], v[2:9], v[244:251], v[118:121], v180, v180 op_sel_hi:[0,0,0]
	v_mfma_scale_f32_16x16x128_f8f6f4 v[114:117], v[10:17], v[244:251], v[114:117], v180, v180 op_sel_hi:[0,0,0]
	v_mfma_scale_f32_16x16x128_f8f6f4 v[142:145], v[18:25], v[212:219], v[142:145], v180, v180 op_sel_hi:[0,0,0]
	v_mfma_scale_f32_16x16x128_f8f6f4 v[138:141], v[26:33], v[212:219], v[138:141], v180, v180 op_sel_hi:[0,0,0]
	v_mfma_scale_f32_16x16x128_f8f6f4 v[134:137], v[18:25], v[222:229], v[134:137], v180, v180 op_sel_hi:[0,0,0]
	v_mfma_scale_f32_16x16x128_f8f6f4 v[130:133], v[26:33], v[222:229], v[130:133], v180, v180 op_sel_hi:[0,0,0]
	v_mfma_scale_f32_16x16x128_f8f6f4 v[110:113], v[18:25], v[236:243], v[110:113], v180, v180 op_sel_hi:[0,0,0]
	v_mfma_scale_f32_16x16x128_f8f6f4 v[106:109], v[26:33], v[236:243], v[106:109], v180, v180 op_sel_hi:[0,0,0]
	v_mfma_scale_f32_16x16x128_f8f6f4 v[102:105], v[18:25], v[244:251], v[102:105], v180, v180 op_sel_hi:[0,0,0]
	v_mfma_scale_f32_16x16x128_f8f6f4 v[98:101], v[26:33], v[244:251], v[98:101], v180, v180 op_sel_hi:[0,0,0]
	s_barrier
	s_mov_b32 m0, s46
	v_lshl_add_u64 v[172:173], v[172:173], 0, s[78:79]
	s_add_u32 s18, s22, 0x20080
	ds_read_b128 v[212:215], v234 offset:49152
	ds_read_b128 v[222:225], v234 offset:51200
	ds_read_b128 v[216:219], v230
	ds_read_b128 v[226:229], v231
	ds_read_b128 v[236:239], v234 offset:53248
	ds_read_b128 v[244:247], v234 offset:55296
	ds_read_b128 v[240:243], v232
	ds_read_b128 v[248:251], v233
	global_load_lds_dwordx4 v[172:173], off
	v_lshl_add_u64 v[172:173], v[174:175], 0, s[78:79]
	s_mov_b32 m0, s48
	s_addc_u32 s19, s23, 0
	global_load_lds_dwordx4 v[172:173], off
	v_lshl_add_u64 v[172:173], s[18:19], 0, v[0:1]
	s_mov_b32 m0, s53
	s_nop 0
	global_load_lds_dwordx4 v[172:173], off
	v_lshl_add_u64 v[172:173], s[18:19], 0, v[162:163]
	s_mov_b32 m0, s54
	s_nop 0
	global_load_lds_dwordx4 v[172:173], off
	v_lshl_add_u64 v[172:173], v[176:177], 0, s[78:79]
	s_mov_b32 m0, s51
	s_nop 0
	global_load_lds_dwordx4 v[172:173], off
	v_lshl_add_u64 v[172:173], v[178:179], 0, s[78:79]
	s_mov_b32 m0, s52
	s_nop 0
	global_load_lds_dwordx4 v[172:173], off
	s_waitcnt vmcnt(8)
	s_waitcnt lgkmcnt(0)
	s_barrier
	s_waitcnt lgkmcnt(0)
	v_mfma_scale_f32_16x16x128_f8f6f4 v[94:97], v[2:9], v[212:219], v[94:97], v180, v180 op_sel_hi:[0,0,0]
	v_mfma_scale_f32_16x16x128_f8f6f4 v[90:93], v[10:17], v[212:219], v[90:93], v180, v180 op_sel_hi:[0,0,0]
	v_mfma_scale_f32_16x16x128_f8f6f4 v[86:89], v[2:9], v[222:229], v[86:89], v180, v180 op_sel_hi:[0,0,0]
	v_mfma_scale_f32_16x16x128_f8f6f4 v[82:85], v[10:17], v[222:229], v[82:85], v180, v180 op_sel_hi:[0,0,0]
	v_mfma_scale_f32_16x16x128_f8f6f4 v[62:65], v[2:9], v[236:243], v[62:65], v180, v180 op_sel_hi:[0,0,0]
	v_mfma_scale_f32_16x16x128_f8f6f4 v[58:61], v[10:17], v[236:243], v[58:61], v180, v180 op_sel_hi:[0,0,0]
	v_mfma_scale_f32_16x16x128_f8f6f4 v[54:57], v[2:9], v[244:251], v[54:57], v180, v180 op_sel_hi:[0,0,0]
	v_mfma_scale_f32_16x16x128_f8f6f4 v[50:53], v[10:17], v[244:251], v[50:53], v180, v180 op_sel_hi:[0,0,0]
	v_mfma_scale_f32_16x16x128_f8f6f4 v[78:81], v[18:25], v[212:219], v[78:81], v180, v180 op_sel_hi:[0,0,0]
	v_mfma_scale_f32_16x16x128_f8f6f4 v[74:77], v[26:33], v[212:219], v[74:77], v180, v180 op_sel_hi:[0,0,0]
	v_mfma_scale_f32_16x16x128_f8f6f4 v[70:73], v[18:25], v[222:229], v[70:73], v180, v180 op_sel_hi:[0,0,0]
	v_mfma_scale_f32_16x16x128_f8f6f4 v[66:69], v[26:33], v[222:229], v[66:69], v180, v180 op_sel_hi:[0,0,0]
	v_mfma_scale_f32_16x16x128_f8f6f4 v[46:49], v[18:25], v[236:243], v[46:49], v180, v180 op_sel_hi:[0,0,0]
	v_mfma_scale_f32_16x16x128_f8f6f4 v[42:45], v[26:33], v[236:243], v[42:45], v180, v180 op_sel_hi:[0,0,0]
	v_mfma_scale_f32_16x16x128_f8f6f4 v[38:41], v[18:25], v[244:251], v[38:41], v180, v180 op_sel_hi:[0,0,0]
	v_mfma_scale_f32_16x16x128_f8f6f4 v[34:37], v[26:33], v[244:251], v[34:37], v180, v180 op_sel_hi:[0,0,0]
	s_barrier
	s_add_i32 s68, s68, 2
	s_add_u32 s13, s13, 0x100
	s_addc_u32 s49, s49, 0
	s_cmp_gt_u32 s68, 5
	s_mov_b64 s[18:19], s[20:21]
.LBB0_1872:
	ds_read_b128 v[18:21], v182
	ds_read_b128 v[26:29], v183
	ds_read_b128 v[22:25], v193
	ds_read_b128 v[30:33], v194
	ds_read_b128 v[2:5], v184
	ds_read_b128 v[10:13], v185
	ds_read_b128 v[6:9], v195
	ds_read_b128 v[14:17], v196
	s_add_u32 s20, s18, 0x100
	s_addc_u32 s21, s19, 0
	s_cmp_eq_u32 s68, 4
	s_cselect_b32 s25, s15, s21
	s_cselect_b32 s24, s14, s20
	s_cselect_b32 s23, s17, s49
	s_cselect_b32 s22, s16, s13
	v_add_u32_e32 v234, 0, v181
	v_lshl_add_u64 v[212:213], s[18:19], 0, v[168:169]
	s_add_i32 m0, s36, 0xc000
	ds_read_b128 v[172:175], v234
	ds_read_b128 v[222:225], v234 offset:2048
	ds_read_b128 v[176:179], v197
	ds_read_b128 v[226:229], v197 offset:2048
	ds_read_b128 v[236:239], v234 offset:4096
	ds_read_b128 v[244:247], v234 offset:6144
	ds_read_b128 v[240:243], v197 offset:4096
	ds_read_b128 v[248:251], v197 offset:6144
	global_load_lds_dwordx4 v[212:213], off
	v_lshl_add_u64 v[212:213], s[18:19], 0, v[170:171]
	s_add_i32 m0, s36, 0xe000
	s_nop 0
	global_load_lds_dwordx4 v[212:213], off
	s_waitcnt vmcnt(8)
	s_waitcnt lgkmcnt(0)
	s_barrier
	s_waitcnt lgkmcnt(0)
	v_mfma_scale_f32_16x16x128_f8f6f4 v[158:161], v[18:25], v[172:179], v[158:161], v180, v180 op_sel_hi:[0,0,0]
	v_mfma_scale_f32_16x16x128_f8f6f4 v[154:157], v[26:33], v[172:179], v[154:157], v180, v180 op_sel_hi:[0,0,0]
	v_mfma_scale_f32_16x16x128_f8f6f4 v[150:153], v[18:25], v[222:229], v[150:153], v180, v180 op_sel_hi:[0,0,0]
	v_mfma_scale_f32_16x16x128_f8f6f4 v[146:149], v[26:33], v[222:229], v[146:149], v180, v180 op_sel_hi:[0,0,0]
	v_mfma_scale_f32_16x16x128_f8f6f4 v[126:129], v[18:25], v[236:243], v[126:129], v180, v180 op_sel_hi:[0,0,0]
	v_mfma_scale_f32_16x16x128_f8f6f4 v[122:125], v[26:33], v[236:243], v[122:125], v180, v180 op_sel_hi:[0,0,0]
	v_mfma_scale_f32_16x16x128_f8f6f4 v[118:121], v[18:25], v[244:251], v[118:121], v180, v180 op_sel_hi:[0,0,0]
	v_mfma_scale_f32_16x16x128_f8f6f4 v[114:117], v[26:33], v[244:251], v[114:117], v180, v180 op_sel_hi:[0,0,0]
	v_mfma_scale_f32_16x16x128_f8f6f4 v[142:145], v[2:9], v[172:179], v[142:145], v180, v180 op_sel_hi:[0,0,0]
	v_mfma_scale_f32_16x16x128_f8f6f4 v[138:141], v[10:17], v[172:179], v[138:141], v180, v180 op_sel_hi:[0,0,0]
	v_mfma_scale_f32_16x16x128_f8f6f4 v[134:137], v[2:9], v[222:229], v[134:137], v180, v180 op_sel_hi:[0,0,0]
	v_mfma_scale_f32_16x16x128_f8f6f4 v[130:133], v[10:17], v[222:229], v[130:133], v180, v180 op_sel_hi:[0,0,0]
	v_mfma_scale_f32_16x16x128_f8f6f4 v[110:113], v[2:9], v[236:243], v[110:113], v180, v180 op_sel_hi:[0,0,0]
	v_mfma_scale_f32_16x16x128_f8f6f4 v[106:109], v[10:17], v[236:243], v[106:109], v180, v180 op_sel_hi:[0,0,0]
	v_mfma_scale_f32_16x16x128_f8f6f4 v[102:105], v[2:9], v[244:251], v[102:105], v180, v180 op_sel_hi:[0,0,0]
	v_mfma_scale_f32_16x16x128_f8f6f4 v[98:101], v[10:17], v[244:251], v[98:101], v180, v180 op_sel_hi:[0,0,0]
	s_barrier
	s_mov_b32 m0, s37
	v_lshl_add_u64 v[172:173], s[22:23], 0, v[0:1]
	s_add_u32 s18, s22, 0x20000
	ds_read_b128 v[222:225], v234 offset:16384
	ds_read_b128 v[236:239], v234 offset:18432
	ds_read_b128 v[226:229], v198
	ds_read_b128 v[240:243], v199
	ds_read_b128 v[244:247], v234 offset:20480
	ds_read_b128 v[212:215], v234 offset:22528
	ds_read_b128 v[248:251], v200
	ds_read_b128 v[216:219], v201
	global_load_lds_dwordx4 v[172:173], off
	v_lshl_add_u64 v[174:175], s[22:23], 0, v[162:163]
	s_mov_b32 m0, s40
	s_addc_u32 s19, s23, 0
	global_load_lds_dwordx4 v[174:175], off
	v_lshl_add_u64 v[176:177], s[18:19], 0, v[0:1]
	s_mov_b32 m0, s41
	v_lshl_add_u64 v[178:179], s[24:25], 0, v[166:167]
	global_load_lds_dwordx4 v[176:177], off
	v_lshl_add_u64 v[176:177], s[18:19], 0, v[162:163]
	s_mov_b32 m0, s42
	s_nop 0
	global_load_lds_dwordx4 v[176:177], off
	v_lshl_add_u64 v[176:177], s[24:25], 0, v[164:165]
	s_mov_b32 m0, s36
	s_nop 0
	global_load_lds_dwordx4 v[176:177], off
	s_mov_b32 m0, s43
	s_nop 0
	global_load_lds_dwordx4 v[178:179], off
	s_waitcnt vmcnt(8)
	s_waitcnt lgkmcnt(0)
	s_barrier
	s_waitcnt lgkmcnt(0)
	v_mfma_scale_f32_16x16x128_f8f6f4 v[94:97], v[18:25], v[222:229], v[94:97], v180, v180 op_sel_hi:[0,0,0]
	v_mfma_scale_f32_16x16x128_f8f6f4 v[90:93], v[26:33], v[222:229], v[90:93], v180, v180 op_sel_hi:[0,0,0]
	v_mfma_scale_f32_16x16x128_f8f6f4 v[86:89], v[18:25], v[236:243], v[86:89], v180, v180 op_sel_hi:[0,0,0]
	v_mfma_scale_f32_16x16x128_f8f6f4 v[82:85], v[26:33], v[236:243], v[82:85], v180, v180 op_sel_hi:[0,0,0]
	v_mfma_scale_f32_16x16x128_f8f6f4 v[62:65], v[18:25], v[244:251], v[62:65], v180, v180 op_sel_hi:[0,0,0]
	v_mfma_scale_f32_16x16x128_f8f6f4 v[58:61], v[26:33], v[244:251], v[58:61], v180, v180 op_sel_hi:[0,0,0]
	v_mfma_scale_f32_16x16x128_f8f6f4 v[54:57], v[18:25], v[212:219], v[54:57], v180, v180 op_sel_hi:[0,0,0]
	v_mfma_scale_f32_16x16x128_f8f6f4 v[50:53], v[26:33], v[212:219], v[50:53], v180, v180 op_sel_hi:[0,0,0]
	v_mfma_scale_f32_16x16x128_f8f6f4 v[78:81], v[2:9], v[222:229], v[78:81], v180, v180 op_sel_hi:[0,0,0]
	v_mfma_scale_f32_16x16x128_f8f6f4 v[74:77], v[10:17], v[222:229], v[74:77], v180, v180 op_sel_hi:[0,0,0]
	v_mfma_scale_f32_16x16x128_f8f6f4 v[70:73], v[2:9], v[236:243], v[70:73], v180, v180 op_sel_hi:[0,0,0]
	v_mfma_scale_f32_16x16x128_f8f6f4 v[66:69], v[10:17], v[236:243], v[66:69], v180, v180 op_sel_hi:[0,0,0]
	v_mfma_scale_f32_16x16x128_f8f6f4 v[46:49], v[2:9], v[244:251], v[46:49], v180, v180 op_sel_hi:[0,0,0]
	v_mfma_scale_f32_16x16x128_f8f6f4 v[42:45], v[10:17], v[244:251], v[42:45], v180, v180 op_sel_hi:[0,0,0]
	v_mfma_scale_f32_16x16x128_f8f6f4 v[38:41], v[2:9], v[212:219], v[38:41], v180, v180 op_sel_hi:[0,0,0]
	v_mfma_scale_f32_16x16x128_f8f6f4 v[34:37], v[10:17], v[212:219], v[34:37], v180, v180 op_sel_hi:[0,0,0]
	s_barrier
	ds_read_b128 v[2:5], v186
	ds_read_b128 v[10:13], v187
	ds_read_b128 v[6:9], v202
	ds_read_b128 v[14:17], v203
	ds_read_b128 v[18:21], v188
	ds_read_b128 v[26:29], v189
	ds_read_b128 v[22:25], v206
	ds_read_b128 v[30:33], v207
	s_add_u32 s18, s24, 0x20000
	s_addc_u32 s19, s25, 0
	s_mov_b32 m0, s44
	v_lshl_add_u64 v[252:253], s[18:19], 0, v[164:165]
	ds_read_b128 v[212:215], v234 offset:32768
	ds_read_b128 v[222:225], v234 offset:34816
	ds_read_b128 v[216:219], v208
	ds_read_b128 v[226:229], v209
	ds_read_b128 v[236:239], v234 offset:36864
	ds_read_b128 v[244:247], v234 offset:38912
	ds_read_b128 v[240:243], v210
	ds_read_b128 v[248:251], v211
	global_load_lds_dwordx4 v[252:253], off
	v_lshl_add_u64 v[252:253], s[18:19], 0, v[166:167]
	s_mov_b32 m0, s45
	s_nop 0
	global_load_lds_dwordx4 v[252:253], off
	s_waitcnt vmcnt(8)
	s_waitcnt lgkmcnt(0)
	s_barrier
	s_waitcnt lgkmcnt(0)
	v_mfma_scale_f32_16x16x128_f8f6f4 v[158:161], v[2:9], v[212:219], v[158:161], v180, v180 op_sel_hi:[0,0,0]
	v_mfma_scale_f32_16x16x128_f8f6f4 v[154:157], v[10:17], v[212:219], v[154:157], v180, v180 op_sel_hi:[0,0,0]
	v_mfma_scale_f32_16x16x128_f8f6f4 v[150:153], v[2:9], v[222:229], v[150:153], v180, v180 op_sel_hi:[0,0,0]
	v_mfma_scale_f32_16x16x128_f8f6f4 v[146:149], v[10:17], v[222:229], v[146:149], v180, v180 op_sel_hi:[0,0,0]
	v_mfma_scale_f32_16x16x128_f8f6f4 v[126:129], v[2:9], v[236:243], v[126:129], v180, v180 op_sel_hi:[0,0,0]
	v_mfma_scale_f32_16x16x128_f8f6f4 v[122:125], v[10:17], v[236:243], v[122:125], v180, v180 op_sel_hi:[0,0,0]
	v_mfma_scale_f32_16x16x128_f8f6f4 v[118:121], v[2:9], v[244:251], v[118:121], v180, v180 op_sel_hi:[0,0,0]
	v_mfma_scale_f32_16x16x128_f8f6f4 v[114:117], v[10:17], v[244:251], v[114:117], v180, v180 op_sel_hi:[0,0,0]
	v_mfma_scale_f32_16x16x128_f8f6f4 v[142:145], v[18:25], v[212:219], v[142:145], v180, v180 op_sel_hi:[0,0,0]
	v_mfma_scale_f32_16x16x128_f8f6f4 v[138:141], v[26:33], v[212:219], v[138:141], v180, v180 op_sel_hi:[0,0,0]
	v_mfma_scale_f32_16x16x128_f8f6f4 v[134:137], v[18:25], v[222:229], v[134:137], v180, v180 op_sel_hi:[0,0,0]
	v_mfma_scale_f32_16x16x128_f8f6f4 v[130:133], v[26:33], v[222:229], v[130:133], v180, v180 op_sel_hi:[0,0,0]
	v_mfma_scale_f32_16x16x128_f8f6f4 v[110:113], v[18:25], v[236:243], v[110:113], v180, v180 op_sel_hi:[0,0,0]
	v_mfma_scale_f32_16x16x128_f8f6f4 v[106:109], v[26:33], v[236:243], v[106:109], v180, v180 op_sel_hi:[0,0,0]
	v_mfma_scale_f32_16x16x128_f8f6f4 v[102:105], v[18:25], v[244:251], v[102:105], v180, v180 op_sel_hi:[0,0,0]
	v_mfma_scale_f32_16x16x128_f8f6f4 v[98:101], v[26:33], v[244:251], v[98:101], v180, v180 op_sel_hi:[0,0,0]
	s_barrier
	s_mov_b32 m0, s46
	v_lshl_add_u64 v[172:173], v[172:173], 0, s[78:79]
	s_add_u32 s18, s22, 0x20080
	ds_read_b128 v[212:215], v234 offset:49152
	ds_read_b128 v[222:225], v234 offset:51200
	ds_read_b128 v[216:219], v230
	ds_read_b128 v[226:229], v231
	ds_read_b128 v[236:239], v234 offset:53248
	ds_read_b128 v[244:247], v234 offset:55296
	ds_read_b128 v[240:243], v232
	ds_read_b128 v[248:251], v233
	global_load_lds_dwordx4 v[172:173], off
	v_lshl_add_u64 v[172:173], v[174:175], 0, s[78:79]
	s_mov_b32 m0, s48
	s_addc_u32 s19, s23, 0
	global_load_lds_dwordx4 v[172:173], off
	v_lshl_add_u64 v[172:173], s[18:19], 0, v[0:1]
	s_mov_b32 m0, s53
	s_nop 0
	global_load_lds_dwordx4 v[172:173], off
	v_lshl_add_u64 v[172:173], s[18:19], 0, v[162:163]
	s_mov_b32 m0, s54
	s_nop 0
	global_load_lds_dwordx4 v[172:173], off
	v_lshl_add_u64 v[172:173], v[176:177], 0, s[78:79]
	s_mov_b32 m0, s51
	s_nop 0
	global_load_lds_dwordx4 v[172:173], off
	v_lshl_add_u64 v[172:173], v[178:179], 0, s[78:79]
	s_mov_b32 m0, s52
	s_nop 0
	global_load_lds_dwordx4 v[172:173], off
	s_waitcnt vmcnt(8)
	s_waitcnt lgkmcnt(0)
	s_barrier
	s_waitcnt lgkmcnt(0)
	v_mfma_scale_f32_16x16x128_f8f6f4 v[94:97], v[2:9], v[212:219], v[94:97], v180, v180 op_sel_hi:[0,0,0]
	v_mfma_scale_f32_16x16x128_f8f6f4 v[90:93], v[10:17], v[212:219], v[90:93], v180, v180 op_sel_hi:[0,0,0]
	v_mfma_scale_f32_16x16x128_f8f6f4 v[86:89], v[2:9], v[222:229], v[86:89], v180, v180 op_sel_hi:[0,0,0]
	v_mfma_scale_f32_16x16x128_f8f6f4 v[82:85], v[10:17], v[222:229], v[82:85], v180, v180 op_sel_hi:[0,0,0]
	v_mfma_scale_f32_16x16x128_f8f6f4 v[62:65], v[2:9], v[236:243], v[62:65], v180, v180 op_sel_hi:[0,0,0]
	v_mfma_scale_f32_16x16x128_f8f6f4 v[58:61], v[10:17], v[236:243], v[58:61], v180, v180 op_sel_hi:[0,0,0]
	v_mfma_scale_f32_16x16x128_f8f6f4 v[54:57], v[2:9], v[244:251], v[54:57], v180, v180 op_sel_hi:[0,0,0]
	v_mfma_scale_f32_16x16x128_f8f6f4 v[50:53], v[10:17], v[244:251], v[50:53], v180, v180 op_sel_hi:[0,0,0]
	v_mfma_scale_f32_16x16x128_f8f6f4 v[78:81], v[18:25], v[212:219], v[78:81], v180, v180 op_sel_hi:[0,0,0]
	v_mfma_scale_f32_16x16x128_f8f6f4 v[74:77], v[26:33], v[212:219], v[74:77], v180, v180 op_sel_hi:[0,0,0]
	v_mfma_scale_f32_16x16x128_f8f6f4 v[70:73], v[18:25], v[222:229], v[70:73], v180, v180 op_sel_hi:[0,0,0]
	v_mfma_scale_f32_16x16x128_f8f6f4 v[66:69], v[26:33], v[222:229], v[66:69], v180, v180 op_sel_hi:[0,0,0]
	v_mfma_scale_f32_16x16x128_f8f6f4 v[46:49], v[18:25], v[236:243], v[46:49], v180, v180 op_sel_hi:[0,0,0]
	v_mfma_scale_f32_16x16x128_f8f6f4 v[42:45], v[26:33], v[236:243], v[42:45], v180, v180 op_sel_hi:[0,0,0]
	v_mfma_scale_f32_16x16x128_f8f6f4 v[38:41], v[18:25], v[244:251], v[38:41], v180, v180 op_sel_hi:[0,0,0]
	v_mfma_scale_f32_16x16x128_f8f6f4 v[34:37], v[26:33], v[244:251], v[34:37], v180, v180 op_sel_hi:[0,0,0]
	s_barrier
	s_add_i32 s68, s68, 2
	s_add_u32 s13, s13, 0x100
	s_addc_u32 s49, s49, 0
	s_cmp_gt_u32 s68, 5
	s_mov_b64 s[18:19], s[20:21]
	s_cbranch_scc0 .LBB0_1872
	s_nop 15
	s_nop 7
	s_and_b64 vcc, exec, s[10:11]
	s_mov_b32 s68, s86
	s_mov_b32 s49, s60
	s_cbranch_vccz .LBB0_1875
	s_barrier

.LBB0_1878:
	s_setprio 0
	s_waitcnt vmcnt(0)
	v_readlane_b32 s54, v254, 5
	v_readlane_b32 s55, v254, 6
	v_readlane_b32 s62, v255, 39
	v_readlane_b32 s66, v255, 41
	s_barrier
	v_readlane_b32 s63, v255, 40
	v_readlane_b32 s67, v255, 42
